# v48 + PEER v-side per-token pick with batched LDS reads
# speedup vs baseline: 1.0049x; 1.0049x over previous
.LBB0_1584:
	s_xor_b64 s[2:3], s[0:1], -1
	s_or_b32 s9, s9, s18
	s_mov_b32 s10, 0
	s_mov_b32 s11, 0
	v_add_u32_e32 v0, 0x1e100, v146
	ds_read_b32 v50, v0
	ds_read_b32 v51, v0 offset:256
	ds_read_b32 v52, v0 offset:512
	ds_read_b32 v53, v0 offset:768
	ds_read_b32 v54, v0 offset:1024
	ds_read_b32 v55, v0 offset:1280
	ds_read_b32 v56, v0 offset:1536
	ds_read_b32 v57, v0 offset:1792
	ds_read_b32 v58, v0 offset:2048
	ds_read_b32 v59, v0 offset:2304
	ds_read_b32 v60, v0 offset:2560
	ds_read_b32 v61, v0 offset:2816
	ds_read_b32 v62, v0 offset:3072
	ds_read_b32 v63, v0 offset:3328
	ds_read_b32 v64, v0 offset:3584
	ds_read_b32 v65, v0 offset:3840
	ds_read_b32 v66, v0 offset:4096
	ds_read_b32 v67, v0 offset:4352
	ds_read_b32 v68, v0 offset:4608
	ds_read_b32 v69, v0 offset:4864
	ds_read_b32 v70, v0 offset:5120
	ds_read_b32 v71, v0 offset:5376
	ds_read_b32 v72, v0 offset:5632
	ds_read_b32 v73, v0 offset:5888
	ds_read_b32 v74, v0 offset:6144
	ds_read_b32 v75, v0 offset:6400
	ds_read_b32 v76, v0 offset:6656
	ds_read_b32 v77, v0 offset:6912
	ds_read_b32 v78, v0 offset:7168
	ds_read_b32 v79, v0 offset:7424
	ds_read_b32 v80, v0 offset:7680
	ds_read_b32 v81, v0 offset:7936
	s_mov_b32 s70, 0x1c100
	s_mov_b32 s68, 0
	s_waitcnt lgkmcnt(15)
	v_and_b32_e32 v1, 0x7ff, v50
	v_lshl_add_u32 v1, v1, 2, s70
	ds_read_b32 v82, v1
	v_and_b32_e32 v1, 0x7ff, v51
	v_lshl_add_u32 v1, v1, 2, s70
	ds_read_b32 v83, v1
	v_and_b32_e32 v1, 0x7ff, v52
	v_lshl_add_u32 v1, v1, 2, s70
	ds_read_b32 v84, v1
	v_and_b32_e32 v1, 0x7ff, v53
	v_lshl_add_u32 v1, v1, 2, s70
	ds_read_b32 v85, v1
	v_and_b32_e32 v1, 0x7ff, v54
	v_lshl_add_u32 v1, v1, 2, s70
	ds_read_b32 v86, v1
	v_and_b32_e32 v1, 0x7ff, v55
	v_lshl_add_u32 v1, v1, 2, s70
	ds_read_b32 v87, v1
	v_and_b32_e32 v1, 0x7ff, v56
	v_lshl_add_u32 v1, v1, 2, s70
	ds_read_b32 v88, v1
	v_and_b32_e32 v1, 0x7ff, v57
	v_lshl_add_u32 v1, v1, 2, s70
	ds_read_b32 v89, v1
	s_waitcnt lgkmcnt(15)
	v_and_b32_e32 v1, 0x7ff, v58
	v_lshl_add_u32 v1, v1, 2, s70
	ds_read_b32 v90, v1
	v_and_b32_e32 v1, 0x7ff, v59
	v_lshl_add_u32 v1, v1, 2, s70
	ds_read_b32 v91, v1
	v_and_b32_e32 v1, 0x7ff, v60
	v_lshl_add_u32 v1, v1, 2, s70
	ds_read_b32 v92, v1
	v_and_b32_e32 v1, 0x7ff, v61
	v_lshl_add_u32 v1, v1, 2, s70
	ds_read_b32 v93, v1
	v_and_b32_e32 v1, 0x7ff, v62
	v_lshl_add_u32 v1, v1, 2, s70
	ds_read_b32 v94, v1
	v_and_b32_e32 v1, 0x7ff, v63
	v_lshl_add_u32 v1, v1, 2, s70
	ds_read_b32 v95, v1
	v_and_b32_e32 v1, 0x7ff, v64
	v_lshl_add_u32 v1, v1, 2, s70
	ds_read_b32 v96, v1
	v_and_b32_e32 v1, 0x7ff, v65
	v_lshl_add_u32 v1, v1, 2, s70
	ds_read_b32 v97, v1
	s_waitcnt lgkmcnt(15)
	v_and_b32_e32 v1, 0x7ff, v66
	v_lshl_add_u32 v1, v1, 2, s70
	ds_read_b32 v98, v1
	v_and_b32_e32 v1, 0x7ff, v67
	v_lshl_add_u32 v1, v1, 2, s70
	ds_read_b32 v99, v1
	v_and_b32_e32 v1, 0x7ff, v68
	v_lshl_add_u32 v1, v1, 2, s70
	ds_read_b32 v100, v1
	v_and_b32_e32 v1, 0x7ff, v69
	v_lshl_add_u32 v1, v1, 2, s70
	ds_read_b32 v101, v1
	v_and_b32_e32 v1, 0x7ff, v70
	v_lshl_add_u32 v1, v1, 2, s70
	ds_read_b32 v102, v1
	v_and_b32_e32 v1, 0x7ff, v71
	v_lshl_add_u32 v1, v1, 2, s70
	ds_read_b32 v103, v1
	v_and_b32_e32 v1, 0x7ff, v72
	v_lshl_add_u32 v1, v1, 2, s70
	ds_read_b32 v104, v1
	v_and_b32_e32 v1, 0x7ff, v73
	v_lshl_add_u32 v1, v1, 2, s70
	ds_read_b32 v105, v1
	s_waitcnt lgkmcnt(7)
	v_and_b32_e32 v1, 0x7ff, v74
	v_lshl_add_u32 v1, v1, 2, s70
	ds_read_b32 v106, v1
	v_and_b32_e32 v1, 0x7ff, v75
	v_lshl_add_u32 v1, v1, 2, s70
	ds_read_b32 v107, v1
	v_and_b32_e32 v1, 0x7ff, v76
	v_lshl_add_u32 v1, v1, 2, s70
	ds_read_b32 v108, v1
	v_and_b32_e32 v1, 0x7ff, v77
	v_lshl_add_u32 v1, v1, 2, s70
	ds_read_b32 v109, v1
	v_and_b32_e32 v1, 0x7ff, v78
	v_lshl_add_u32 v1, v1, 2, s70
	ds_read_b32 v110, v1
	v_and_b32_e32 v1, 0x7ff, v79
	v_lshl_add_u32 v1, v1, 2, s70
	ds_read_b32 v111, v1
	v_and_b32_e32 v1, 0x7ff, v80
	v_lshl_add_u32 v1, v1, 2, s70
	ds_read_b32 v112, v1
	v_and_b32_e32 v1, 0x7ff, v81
	v_lshl_add_u32 v1, v1, 2, s70
	ds_read_b32 v113, v1
	s_waitcnt lgkmcnt(0)
	v_bfe_u32 v2, v50, 7, 4
	v_bfe_u32 v3, v51, 7, 4
	v_bfe_u32 v4, v52, 7, 4
	v_bfe_u32 v5, v53, 7, 4
	v_cmp_eq_u32_e64 s[58:59], s9, v2
	v_cmp_eq_u32_e64 s[60:61], s9, v3
	v_cmp_eq_u32_e64 s[62:63], s9, v4
	v_cmp_eq_u32_e64 s[64:65], s9, v5
	s_bcnt1_i32_b64 s69, s[58:59]
	v_mbcnt_lo_u32_b32 v1, s58, 0
	v_mbcnt_hi_u32_b32 v1, s59, v1
	v_add_u32_e32 v1, s68, v1
	v_lshrrev_b32_e32 v6, 11, v50
	v_lshl_add_u32 v1, v1, 2, s17
	s_mov_b64 exec, s[58:59]
	ds_write2st64_b32 v1, v6, v82 offset1:2
	s_mov_b64 exec, -1
	s_add_u32 s68, s68, s69
	s_bcnt1_i32_b64 s69, s[60:61]
	v_mbcnt_lo_u32_b32 v1, s60, 0
	v_mbcnt_hi_u32_b32 v1, s61, v1
	v_add_u32_e32 v1, s68, v1
	v_lshrrev_b32_e32 v6, 11, v51
	v_lshl_add_u32 v1, v1, 2, s17
	s_mov_b64 exec, s[60:61]
	ds_write2st64_b32 v1, v6, v83 offset1:2
	s_mov_b64 exec, -1
	s_add_u32 s68, s68, s69
	s_bcnt1_i32_b64 s69, s[62:63]
	v_mbcnt_lo_u32_b32 v1, s62, 0
	v_mbcnt_hi_u32_b32 v1, s63, v1
	v_add_u32_e32 v1, s68, v1
	v_lshrrev_b32_e32 v6, 11, v52
	v_lshl_add_u32 v1, v1, 2, s17
	s_mov_b64 exec, s[62:63]
	ds_write2st64_b32 v1, v6, v84 offset1:2
	s_mov_b64 exec, -1
	s_add_u32 s68, s68, s69
	s_bcnt1_i32_b64 s69, s[64:65]
	v_mbcnt_lo_u32_b32 v1, s64, 0
	v_mbcnt_hi_u32_b32 v1, s65, v1
	v_add_u32_e32 v1, s68, v1
	v_lshrrev_b32_e32 v6, 11, v53
	v_lshl_add_u32 v1, v1, 2, s17
	s_mov_b64 exec, s[64:65]
	ds_write2st64_b32 v1, v6, v85 offset1:2
	s_mov_b64 exec, -1
	s_add_u32 s68, s68, s69
	v_bfe_u32 v2, v54, 7, 4
	v_bfe_u32 v3, v55, 7, 4
	v_bfe_u32 v4, v56, 7, 4
	v_bfe_u32 v5, v57, 7, 4
	v_cmp_eq_u32_e64 s[58:59], s9, v2
	v_cmp_eq_u32_e64 s[60:61], s9, v3
	v_cmp_eq_u32_e64 s[62:63], s9, v4
	v_cmp_eq_u32_e64 s[64:65], s9, v5
	s_bcnt1_i32_b64 s69, s[58:59]
	v_mbcnt_lo_u32_b32 v1, s58, 0
	v_mbcnt_hi_u32_b32 v1, s59, v1
	v_add_u32_e32 v1, s68, v1
	v_lshrrev_b32_e32 v6, 11, v54
	v_lshl_add_u32 v1, v1, 2, s17
	s_mov_b64 exec, s[58:59]
	ds_write2st64_b32 v1, v6, v86 offset1:2
	s_mov_b64 exec, -1
	s_add_u32 s68, s68, s69
	s_bcnt1_i32_b64 s69, s[60:61]
	v_mbcnt_lo_u32_b32 v1, s60, 0
	v_mbcnt_hi_u32_b32 v1, s61, v1
	v_add_u32_e32 v1, s68, v1
	v_lshrrev_b32_e32 v6, 11, v55
	v_lshl_add_u32 v1, v1, 2, s17
	s_mov_b64 exec, s[60:61]
	ds_write2st64_b32 v1, v6, v87 offset1:2
	s_mov_b64 exec, -1
	s_add_u32 s68, s68, s69
	s_bcnt1_i32_b64 s69, s[62:63]
	v_mbcnt_lo_u32_b32 v1, s62, 0
	v_mbcnt_hi_u32_b32 v1, s63, v1
	v_add_u32_e32 v1, s68, v1
	v_lshrrev_b32_e32 v6, 11, v56
	v_lshl_add_u32 v1, v1, 2, s17
	s_mov_b64 exec, s[62:63]
	ds_write2st64_b32 v1, v6, v88 offset1:2
	s_mov_b64 exec, -1
	s_add_u32 s68, s68, s69
	s_bcnt1_i32_b64 s69, s[64:65]
	v_mbcnt_lo_u32_b32 v1, s64, 0
	v_mbcnt_hi_u32_b32 v1, s65, v1
	v_add_u32_e32 v1, s68, v1
	v_lshrrev_b32_e32 v6, 11, v57
	v_lshl_add_u32 v1, v1, 2, s17
	s_mov_b64 exec, s[64:65]
	ds_write2st64_b32 v1, v6, v89 offset1:2
	s_mov_b64 exec, -1
	s_add_u32 s68, s68, s69
	v_bfe_u32 v2, v58, 7, 4
	v_bfe_u32 v3, v59, 7, 4
	v_bfe_u32 v4, v60, 7, 4
	v_bfe_u32 v5, v61, 7, 4
	v_cmp_eq_u32_e64 s[58:59], s9, v2
	v_cmp_eq_u32_e64 s[60:61], s9, v3
	v_cmp_eq_u32_e64 s[62:63], s9, v4
	v_cmp_eq_u32_e64 s[64:65], s9, v5
	s_bcnt1_i32_b64 s69, s[58:59]
	v_mbcnt_lo_u32_b32 v1, s58, 0
	v_mbcnt_hi_u32_b32 v1, s59, v1
	v_add_u32_e32 v1, s68, v1
	v_lshrrev_b32_e32 v6, 11, v58
	v_lshl_add_u32 v1, v1, 2, s17
	s_mov_b64 exec, s[58:59]
	ds_write2st64_b32 v1, v6, v90 offset1:2
	s_mov_b64 exec, -1
	s_add_u32 s68, s68, s69
	s_bcnt1_i32_b64 s69, s[60:61]
	v_mbcnt_lo_u32_b32 v1, s60, 0
	v_mbcnt_hi_u32_b32 v1, s61, v1
	v_add_u32_e32 v1, s68, v1
	v_lshrrev_b32_e32 v6, 11, v59
	v_lshl_add_u32 v1, v1, 2, s17
	s_mov_b64 exec, s[60:61]
	ds_write2st64_b32 v1, v6, v91 offset1:2
	s_mov_b64 exec, -1
	s_add_u32 s68, s68, s69
	s_bcnt1_i32_b64 s69, s[62:63]
	v_mbcnt_lo_u32_b32 v1, s62, 0
	v_mbcnt_hi_u32_b32 v1, s63, v1
	v_add_u32_e32 v1, s68, v1
	v_lshrrev_b32_e32 v6, 11, v60
	v_lshl_add_u32 v1, v1, 2, s17
	s_mov_b64 exec, s[62:63]
	ds_write2st64_b32 v1, v6, v92 offset1:2
	s_mov_b64 exec, -1
	s_add_u32 s68, s68, s69
	s_bcnt1_i32_b64 s69, s[64:65]
	v_mbcnt_lo_u32_b32 v1, s64, 0
	v_mbcnt_hi_u32_b32 v1, s65, v1
	v_add_u32_e32 v1, s68, v1
	v_lshrrev_b32_e32 v6, 11, v61
	v_lshl_add_u32 v1, v1, 2, s17
	s_mov_b64 exec, s[64:65]
	ds_write2st64_b32 v1, v6, v93 offset1:2
	s_mov_b64 exec, -1
	s_add_u32 s68, s68, s69
	v_bfe_u32 v2, v62, 7, 4
	v_bfe_u32 v3, v63, 7, 4
	v_bfe_u32 v4, v64, 7, 4
	v_bfe_u32 v5, v65, 7, 4
	v_cmp_eq_u32_e64 s[58:59], s9, v2
	v_cmp_eq_u32_e64 s[60:61], s9, v3
	v_cmp_eq_u32_e64 s[62:63], s9, v4
	v_cmp_eq_u32_e64 s[64:65], s9, v5
	s_bcnt1_i32_b64 s69, s[58:59]
	v_mbcnt_lo_u32_b32 v1, s58, 0
	v_mbcnt_hi_u32_b32 v1, s59, v1
	v_add_u32_e32 v1, s68, v1
	v_lshrrev_b32_e32 v6, 11, v62
	v_lshl_add_u32 v1, v1, 2, s17
	s_mov_b64 exec, s[58:59]
	ds_write2st64_b32 v1, v6, v94 offset1:2
	s_mov_b64 exec, -1
	s_add_u32 s68, s68, s69
	s_bcnt1_i32_b64 s69, s[60:61]
	v_mbcnt_lo_u32_b32 v1, s60, 0
	v_mbcnt_hi_u32_b32 v1, s61, v1
	v_add_u32_e32 v1, s68, v1
	v_lshrrev_b32_e32 v6, 11, v63
	v_lshl_add_u32 v1, v1, 2, s17
	s_mov_b64 exec, s[60:61]
	ds_write2st64_b32 v1, v6, v95 offset1:2
	s_mov_b64 exec, -1
	s_add_u32 s68, s68, s69
	s_bcnt1_i32_b64 s69, s[62:63]
	v_mbcnt_lo_u32_b32 v1, s62, 0
	v_mbcnt_hi_u32_b32 v1, s63, v1
	v_add_u32_e32 v1, s68, v1
	v_lshrrev_b32_e32 v6, 11, v64
	v_lshl_add_u32 v1, v1, 2, s17
	s_mov_b64 exec, s[62:63]
	ds_write2st64_b32 v1, v6, v96 offset1:2
	s_mov_b64 exec, -1
	s_add_u32 s68, s68, s69
	s_bcnt1_i32_b64 s69, s[64:65]
	v_mbcnt_lo_u32_b32 v1, s64, 0
	v_mbcnt_hi_u32_b32 v1, s65, v1
	v_add_u32_e32 v1, s68, v1
	v_lshrrev_b32_e32 v6, 11, v65
	v_lshl_add_u32 v1, v1, 2, s17
	s_mov_b64 exec, s[64:65]
	ds_write2st64_b32 v1, v6, v97 offset1:2
	s_mov_b64 exec, -1
	s_add_u32 s68, s68, s69
	v_bfe_u32 v2, v66, 7, 4
	v_bfe_u32 v3, v67, 7, 4
	v_bfe_u32 v4, v68, 7, 4
	v_bfe_u32 v5, v69, 7, 4
	v_cmp_eq_u32_e64 s[58:59], s9, v2
	v_cmp_eq_u32_e64 s[60:61], s9, v3
	v_cmp_eq_u32_e64 s[62:63], s9, v4
	v_cmp_eq_u32_e64 s[64:65], s9, v5
	s_bcnt1_i32_b64 s69, s[58:59]
	v_mbcnt_lo_u32_b32 v1, s58, 0
	v_mbcnt_hi_u32_b32 v1, s59, v1
	v_add_u32_e32 v1, s68, v1
	v_lshrrev_b32_e32 v6, 11, v66
	v_lshl_add_u32 v1, v1, 2, s17
	s_mov_b64 exec, s[58:59]
	ds_write2st64_b32 v1, v6, v98 offset1:2
	s_mov_b64 exec, -1
	s_add_u32 s68, s68, s69
	s_bcnt1_i32_b64 s69, s[60:61]
	v_mbcnt_lo_u32_b32 v1, s60, 0
	v_mbcnt_hi_u32_b32 v1, s61, v1
	v_add_u32_e32 v1, s68, v1
	v_lshrrev_b32_e32 v6, 11, v67
	v_lshl_add_u32 v1, v1, 2, s17
	s_mov_b64 exec, s[60:61]
	ds_write2st64_b32 v1, v6, v99 offset1:2
	s_mov_b64 exec, -1
	s_add_u32 s68, s68, s69
	s_bcnt1_i32_b64 s69, s[62:63]
	v_mbcnt_lo_u32_b32 v1, s62, 0
	v_mbcnt_hi_u32_b32 v1, s63, v1
	v_add_u32_e32 v1, s68, v1
	v_lshrrev_b32_e32 v6, 11, v68
	v_lshl_add_u32 v1, v1, 2, s17
	s_mov_b64 exec, s[62:63]
	ds_write2st64_b32 v1, v6, v100 offset1:2
	s_mov_b64 exec, -1
	s_add_u32 s68, s68, s69
	s_bcnt1_i32_b64 s69, s[64:65]
	v_mbcnt_lo_u32_b32 v1, s64, 0
	v_mbcnt_hi_u32_b32 v1, s65, v1
	v_add_u32_e32 v1, s68, v1
	v_lshrrev_b32_e32 v6, 11, v69
	v_lshl_add_u32 v1, v1, 2, s17
	s_mov_b64 exec, s[64:65]
	ds_write2st64_b32 v1, v6, v101 offset1:2
	s_mov_b64 exec, -1
	s_add_u32 s68, s68, s69
	v_bfe_u32 v2, v70, 7, 4
	v_bfe_u32 v3, v71, 7, 4
	v_bfe_u32 v4, v72, 7, 4
	v_bfe_u32 v5, v73, 7, 4
	v_cmp_eq_u32_e64 s[58:59], s9, v2
	v_cmp_eq_u32_e64 s[60:61], s9, v3
	v_cmp_eq_u32_e64 s[62:63], s9, v4
	v_cmp_eq_u32_e64 s[64:65], s9, v5
	s_bcnt1_i32_b64 s69, s[58:59]
	v_mbcnt_lo_u32_b32 v1, s58, 0
	v_mbcnt_hi_u32_b32 v1, s59, v1
	v_add_u32_e32 v1, s68, v1
	v_lshrrev_b32_e32 v6, 11, v70
	v_lshl_add_u32 v1, v1, 2, s17
	s_mov_b64 exec, s[58:59]
	ds_write2st64_b32 v1, v6, v102 offset1:2
	s_mov_b64 exec, -1
	s_add_u32 s68, s68, s69
	s_bcnt1_i32_b64 s69, s[60:61]
	v_mbcnt_lo_u32_b32 v1, s60, 0
	v_mbcnt_hi_u32_b32 v1, s61, v1
	v_add_u32_e32 v1, s68, v1
	v_lshrrev_b32_e32 v6, 11, v71
	v_lshl_add_u32 v1, v1, 2, s17
	s_mov_b64 exec, s[60:61]
	ds_write2st64_b32 v1, v6, v103 offset1:2
	s_mov_b64 exec, -1
	s_add_u32 s68, s68, s69
	s_bcnt1_i32_b64 s69, s[62:63]
	v_mbcnt_lo_u32_b32 v1, s62, 0
	v_mbcnt_hi_u32_b32 v1, s63, v1
	v_add_u32_e32 v1, s68, v1
	v_lshrrev_b32_e32 v6, 11, v72
	v_lshl_add_u32 v1, v1, 2, s17
	s_mov_b64 exec, s[62:63]
	ds_write2st64_b32 v1, v6, v104 offset1:2
	s_mov_b64 exec, -1
	s_add_u32 s68, s68, s69
	s_bcnt1_i32_b64 s69, s[64:65]
	v_mbcnt_lo_u32_b32 v1, s64, 0
	v_mbcnt_hi_u32_b32 v1, s65, v1
	v_add_u32_e32 v1, s68, v1
	v_lshrrev_b32_e32 v6, 11, v73
	v_lshl_add_u32 v1, v1, 2, s17
	s_mov_b64 exec, s[64:65]
	ds_write2st64_b32 v1, v6, v105 offset1:2
	s_mov_b64 exec, -1
	s_add_u32 s68, s68, s69
	v_bfe_u32 v2, v74, 7, 4
	v_bfe_u32 v3, v75, 7, 4
	v_bfe_u32 v4, v76, 7, 4
	v_bfe_u32 v5, v77, 7, 4
	v_cmp_eq_u32_e64 s[58:59], s9, v2
	v_cmp_eq_u32_e64 s[60:61], s9, v3
	v_cmp_eq_u32_e64 s[62:63], s9, v4
	v_cmp_eq_u32_e64 s[64:65], s9, v5
	s_bcnt1_i32_b64 s69, s[58:59]
	v_mbcnt_lo_u32_b32 v1, s58, 0
	v_mbcnt_hi_u32_b32 v1, s59, v1
	v_add_u32_e32 v1, s68, v1
	v_lshrrev_b32_e32 v6, 11, v74
	v_lshl_add_u32 v1, v1, 2, s17
	s_mov_b64 exec, s[58:59]
	ds_write2st64_b32 v1, v6, v106 offset1:2
	s_mov_b64 exec, -1
	s_add_u32 s68, s68, s69
	s_bcnt1_i32_b64 s69, s[60:61]
	v_mbcnt_lo_u32_b32 v1, s60, 0
	v_mbcnt_hi_u32_b32 v1, s61, v1
	v_add_u32_e32 v1, s68, v1
	v_lshrrev_b32_e32 v6, 11, v75
	v_lshl_add_u32 v1, v1, 2, s17
	s_mov_b64 exec, s[60:61]
	ds_write2st64_b32 v1, v6, v107 offset1:2
	s_mov_b64 exec, -1
	s_add_u32 s68, s68, s69
	s_bcnt1_i32_b64 s69, s[62:63]
	v_mbcnt_lo_u32_b32 v1, s62, 0
	v_mbcnt_hi_u32_b32 v1, s63, v1
	v_add_u32_e32 v1, s68, v1
	v_lshrrev_b32_e32 v6, 11, v76
	v_lshl_add_u32 v1, v1, 2, s17
	s_mov_b64 exec, s[62:63]
	ds_write2st64_b32 v1, v6, v108 offset1:2
	s_mov_b64 exec, -1
	s_add_u32 s68, s68, s69
	s_bcnt1_i32_b64 s69, s[64:65]
	v_mbcnt_lo_u32_b32 v1, s64, 0
	v_mbcnt_hi_u32_b32 v1, s65, v1
	v_add_u32_e32 v1, s68, v1
	v_lshrrev_b32_e32 v6, 11, v77
	v_lshl_add_u32 v1, v1, 2, s17
	s_mov_b64 exec, s[64:65]
	ds_write2st64_b32 v1, v6, v109 offset1:2
	s_mov_b64 exec, -1
	s_add_u32 s68, s68, s69
	v_bfe_u32 v2, v78, 7, 4
	v_bfe_u32 v3, v79, 7, 4
	v_bfe_u32 v4, v80, 7, 4
	v_bfe_u32 v5, v81, 7, 4
	v_cmp_eq_u32_e64 s[58:59], s9, v2
	v_cmp_eq_u32_e64 s[60:61], s9, v3
	v_cmp_eq_u32_e64 s[62:63], s9, v4
	v_cmp_eq_u32_e64 s[64:65], s9, v5
	s_bcnt1_i32_b64 s69, s[58:59]
	v_mbcnt_lo_u32_b32 v1, s58, 0
	v_mbcnt_hi_u32_b32 v1, s59, v1
	v_add_u32_e32 v1, s68, v1
	v_lshrrev_b32_e32 v6, 11, v78
	v_lshl_add_u32 v1, v1, 2, s17
	s_mov_b64 exec, s[58:59]
	ds_write2st64_b32 v1, v6, v110 offset1:2
	s_mov_b64 exec, -1
	s_add_u32 s68, s68, s69
	s_bcnt1_i32_b64 s69, s[60:61]
	v_mbcnt_lo_u32_b32 v1, s60, 0
	v_mbcnt_hi_u32_b32 v1, s61, v1
	v_add_u32_e32 v1, s68, v1
	v_lshrrev_b32_e32 v6, 11, v79
	v_lshl_add_u32 v1, v1, 2, s17
	s_mov_b64 exec, s[60:61]
	ds_write2st64_b32 v1, v6, v111 offset1:2
	s_mov_b64 exec, -1
	s_add_u32 s68, s68, s69
	s_bcnt1_i32_b64 s69, s[62:63]
	v_mbcnt_lo_u32_b32 v1, s62, 0
	v_mbcnt_hi_u32_b32 v1, s63, v1
	v_add_u32_e32 v1, s68, v1
	v_lshrrev_b32_e32 v6, 11, v80
	v_lshl_add_u32 v1, v1, 2, s17
	s_mov_b64 exec, s[62:63]
	ds_write2st64_b32 v1, v6, v112 offset1:2
	s_mov_b64 exec, -1
	s_add_u32 s68, s68, s69
	s_bcnt1_i32_b64 s69, s[64:65]
	v_mbcnt_lo_u32_b32 v1, s64, 0
	v_mbcnt_hi_u32_b32 v1, s65, v1
	v_add_u32_e32 v1, s68, v1
	v_lshrrev_b32_e32 v6, 11, v81
	v_lshl_add_u32 v1, v1, 2, s17
	s_mov_b64 exec, s[64:65]
	ds_write2st64_b32 v1, v6, v113 offset1:2
	s_mov_b64 exec, -1
	s_add_u32 s68, s68, s69
